# speedup vs baseline: 1.0329x; 1.0097x over previous
.Lk2f_i2:
	s_mov_b64 exec, s[6:7]
	s_waitcnt lgkmcnt(0)
	v_mov_b32_e32 v8, 0
	v_mov_b32_e32 v9, 0
	s_cmp_lt_u32 s4, 4
	s_cbranch_scc0 .Lk2f_l3
	s_movk_i32 s5, 0xf5
	v_cmp_gt_u32_e32 vcc, s5, v0
	v_mov_b32_e32 v23, s3
	s_movk_i32 s5, 0x3fe
	v_mad_u32_u24 v23, v0, s5, v23
	v_lshlrev_b32_e32 v23, 2, v23
	s_and_saveexec_b64 s[6:7], vcc
	global_load_dwordx2 v[8:9], v23, s[12:13]
	s_mov_b64 exec, s[6:7]
.Lk2f_l3:
	v_add_u32_e32 v25, 0x2000, v2
	global_load_dwordx4 v[10:13], v2, s[18:19]
	global_load_dwordx4 v[14:17], v25, s[18:19]
	s_load_dwordx2 s[36:37], s[24:25], 0x0
	s_cmp_lt_u32 s4, 2
	s_cbranch_scc0 .Lk2f_l1
	global_load_dwordx4 v[18:21], v2, s[20:21]

.Lk2f_l2:
	s_cmp_lt_u32 s4, 4
	s_cbranch_scc0 .Lk2f_l4w
	s_cmp_lt_u32 s4, 2
	s_cbranch_scc1 .Lk2f_w3
	s_waitcnt vmcnt(2)
	s_branch .Lk2f_wd

.Lk2f_wd:
	v_sub_u32_e32 v24, v9, v8
	v_min_u32_e32 v25, 0xf4, v0
	v_lshlrev_b32_e32 v25, 14, v25
	v_lshl_add_u32 v25, v8, 2, v25
	global_load_dwordx4 v[26:29], v25, s[10:11]
	global_load_dwordx4 v[30:33], v25, s[10:11] offset:16
	global_load_dwordx4 v[34:37], v25, s[10:11] offset:32
	global_load_dwordx4 v[38:41], v25, s[10:11] offset:48
	v_add_u32_dpp v42, v8, v8 row_shr:1 row_mask:0xf bank_mask:0xf bound_ctrl:1
	s_nop 1
	v_add_u32_dpp v42, v42, v42 row_shr:2 row_mask:0xf bank_mask:0xf bound_ctrl:1
	s_nop 1
	v_add_u32_dpp v42, v42, v42 row_shr:4 row_mask:0xf bank_mask:0xf bound_ctrl:1
	s_nop 1
	v_add_u32_dpp v42, v42, v42 row_shr:8 row_mask:0xf bank_mask:0xf bound_ctrl:1
	s_nop 1
	v_add_u32_dpp v42, v42, v42 row_bcast:15 row_mask:0xa bank_mask:0xf
	s_nop 1
	v_add_u32_dpp v42, v42, v42 row_bcast:31 row_mask:0xc bank_mask:0xf
	s_lshl_b32 s5, s4, 2
	v_mov_b32_e32 v43, s5
	v_readlane_b32 s5, v42, 63
	s_nop 3
	v_mov_b32_e32 v42, s5
	ds_write_b32 v43, v42 offset:19216
	s_waitcnt vmcnt(4)
	s_branch .Lk2f_l4
.Lk2f_l4w:
	s_waitcnt vmcnt(0)
.Lk2f_l4:
	ds_write_b128 v2, v[10:13]
	ds_write_b128 v2, v[14:17] offset:8192
	s_cmp_lt_u32 s4, 2
	s_cbranch_scc0 .Lk2f_l5
	ds_write_b128 v2, v[18:21] offset:16384
